# MoBA tile loops: first four K-fragment ds_reads hoisted directly behind the per-tile barrier, ahead of the scalar need logic
# baseline (speedup 1.0000x reference)
.LBB0_487:
	s_waitcnt vmcnt(2) lgkmcnt(0)
	s_barrier
	v_add_u32_e32 v160, s33, v165
	ds_read_b128 v[80:83], v160
	ds_read_b128 v[84:87], v160 offset:512
	ds_read_b128 v[88:91], v160 offset:2048
	ds_read_b128 v[96:99], v160 offset:2560

.LBB0_493:
	s_andn2_b64 vcc, exec, s[6:7]
	s_andn2_b64 s[6:7], s[44:45], exec
	s_and_b64 s[46:47], s[44:45], exec
	s_or_b64 s[46:47], s[6:7], s[46:47]
	s_cbranch_vccnz .LBB0_485
	v_add_u32_e32 v32, s56, v199
	v_cvt_f32_i32_e32 v32, v32
	s_lshl_b32 s6, 1, s52
	s_add_i32 s32, s51, 2
	s_cmp_ge_u32 s32, s57
	s_cbranch_scc1 .Lmoba0_a
	s_add_i32 s32, s18, s50
	s_mov_b32 m0, s32
	s_nop 0
	global_load_lds_dwordx4 v[156:157], off
	s_add_i32 m0, s32, 0x6000
	s_nop 0
	global_load_lds_dwordx4 v[158:159], off

.LBB0_3026:
	s_waitcnt vmcnt(2) lgkmcnt(0)
	s_barrier
	v_add_u32_e32 v160, s36, v165
	ds_read_b128 v[80:83], v160
	ds_read_b128 v[88:91], v160 offset:512
	ds_read_b128 v[96:99], v160 offset:2048
	ds_read_b128 v[104:107], v160 offset:2560

.LBB0_3032:
	s_andn2_b64 vcc, exec, s[6:7]
	s_andn2_b64 s[6:7], s[30:31], exec
	s_and_b64 s[34:35], s[30:31], exec
	s_or_b64 s[34:35], s[6:7], s[34:35]
	s_cbranch_vccnz .LBB0_3024
	v_add_u32_e32 v32, s56, v199
	v_cvt_f32_i32_e32 v32, v32
	s_lshl_b32 s6, 1, s41
	s_add_i32 s32, s40, 2
	s_cmp_ge_u32 s32, s57
	s_cbranch_scc1 .Lmoba1_a
	s_add_i32 s32, s43, s39
	s_mov_b32 m0, s32
	s_nop 0
	global_load_lds_dwordx4 v[156:157], off
	s_add_i32 m0, s32, 0x6000
	s_nop 0
	global_load_lds_dwordx4 v[158:159], off
